# speedup vs baseline: 1.0618x; 1.0089x over previous
.Lm_nok_p1:
	s_waitcnt vmcnt(2)
	s_nop 0
	v_max3_f32 v132, v132, v133, v134
	v_max3_f32 v136, v136, v137, v138
	v_max3_f32 v132, v132, v135, v139
	v_max3_f32 v132, v132, v136, v140
	s_nop 1
	v_max_f32_dpp v132, v132, v132 quad_perm:[1,0,3,2] row_mask:0xf bank_mask:0xf
	s_nop 1
	v_max_f32_dpp v132, v132, v132 quad_perm:[2,3,0,1] row_mask:0xf bank_mask:0xf
	s_nop 1
	v_max_f32_dpp v132, v132, v132 row_half_mirror row_mask:0xf bank_mask:0xf
	s_nop 1
	v_max_f32_dpp v132, v132, v132 row_mirror row_mask:0xf bank_mask:0xf
	s_nop 1
	v_readlane_b32 s36, v132, 0
	v_readlane_b32 s37, v132, 16
	v_readlane_b32 s38, v132, 32
	v_readlane_b32 s39, v132, 48
	s_nop 2
	v_mov_b32_e32 v133, s36
	v_max_f32_e32 v133, s37, v133
	v_max_f32_e32 v133, s38, v133
	v_max_f32_e32 v133, s39, v133
	s_mov_b32 s37, 0xf800000
	v_mul_f32_e32 v137, 0x4f800000, v133
	v_cmp_gt_f32_e32 vcc, s37, v133
	s_nop 1
	v_cndmask_b32_e32 v133, v133, v137, vcc
	v_sqrt_f32_e32 v137, v133
	s_nop 0
	v_add_u32_e32 v138, -1, v137
	v_add_u32_e32 v139, 1, v137
	v_fma_f32 v143, -v138, v137, v133
	v_fma_f32 v144, -v139, v137, v133
	v_cmp_ge_f32_e64 s[38:39], 0, v143
	s_nop 1
	v_cndmask_b32_e64 v137, v137, v138, s[38:39]
	v_cmp_lt_f32_e64 s[38:39], 0, v144
	s_nop 1
	v_cndmask_b32_e64 v137, v137, v139, s[38:39]
	v_mul_f32_e32 v138, 0x37800000, v137
	v_cndmask_b32_e32 v137, v137, v138, vcc
	v_mov_b32_e32 v138, 0x260
	v_cmp_class_f32_e32 vcc, v133, v138
	s_nop 1
	v_cndmask_b32_e32 v133, v137, v133, vcc
	v_mov_b32_e32 v135, 0x3ca3d70a
	s_mov_b32 s36, 0xffff
	v_mul_f32_e32 v134, v141, v133
	v_mul_f32_e32 v136, v142, v133
	v_fmamk_f32 v134, v134, 0x3f804189, v135
	v_fmamk_f32 v136, v136, 0x3f804189, v135
	v_cvt_f16_f32_e64 v134, -v134
	v_cvt_f16_f32_e64 v136, -v136
	v_cmp_gt_u32_e32 vcc, 32, v1
	v_cvt_f32_f16_e32 v148, v134
	v_cvt_f32_f16_e32 v149, v136
	v_bfi_b32 v134, s36, v134, v11
	v_bfi_b32 v136, s36, v136, v15
	v_cndmask_b32_e32 v11, v11, v134, vcc
	v_cndmask_b32_e32 v15, v15, v136, vcc
	v_mov_b32_e32 v16, 0
	v_mov_b32_e32 v17, 0
	v_mov_b32_e32 v18, 0
	v_mov_b32_e32 v19, 0
	v_mov_b32_e32 v20, 0
	v_mov_b32_e32 v21, 0
	v_mov_b32_e32 v22, 0
	v_mov_b32_e32 v23, 0
	v_mov_b32_e32 v24, 0
	v_mov_b32_e32 v25, 0
	v_mov_b32_e32 v26, 0
	v_mov_b32_e32 v27, 0
	v_mov_b32_e32 v28, 0
	v_mov_b32_e32 v29, 0
	v_mov_b32_e32 v30, 0
	v_mov_b32_e32 v31, 0
	v_mov_b32_e32 v32, 0
	v_mov_b32_e32 v33, 0
	v_mov_b32_e32 v34, 0
	v_mov_b32_e32 v35, 0
	v_mov_b32_e32 v36, 0
	v_mov_b32_e32 v37, 0
	v_mov_b32_e32 v38, 0
	v_mov_b32_e32 v39, 0
	v_mov_b32_e32 v40, 0
	v_mov_b32_e32 v41, 0
	v_mov_b32_e32 v42, 0
	v_mov_b32_e32 v43, 0
	v_mov_b32_e32 v44, 0
	v_mov_b32_e32 v45, 0
	v_mov_b32_e32 v46, 0
	v_mov_b32_e32 v47, 0
	s_waitcnt vmcnt(0)
	s_barrier
	s_mov_b32 s28, 2
	s_sub_u32 s30, s28, s25
	s_mul_i32 s30, s30, 6
	s_add_u32 s30, s30, s24
	s_mul_i32 s31, s28, 6
	s_add_u32 s31, s31, s22
	s_cmp_lt_u32 s28, s25
	s_cselect_b32 s30, s31, s30
	s_lshl_b32 s33, s18, 10
	s_lshl_b32 s31, s30, 12
	s_add_u32 s31, s31, s33
	s_add_u32 s50, s8, s31
	s_addc_u32 s51, s9, 0
	s_add_u32 s52, s50, 0x3000
	s_addc_u32 s53, s51, 0
	s_add_u32 s34, s48, s33
	s_mov_b32 m0, s34
	s_add_u32 s35, s34, 0x3000
	global_load_lds_dwordx4 v2, s[50:51]
	s_mov_b32 m0, s35
	s_nop 0
	global_load_lds_dwordx4 v2, s[52:53]
	s_cmp_lt_u32 s18, 6
	s_cbranch_scc0 .Lm_nok_p2
	s_lshl_b32 s31, s30, 10
	s_add_u32 s31, s31, s33
	s_add_u32 s54, s4, s31
	s_addc_u32 s55, s5, 0
	s_add_u32 s34, s34, 24576
	s_mov_b32 m0, s34
	s_nop 0
	global_load_lds_dwordx4 v2, s[54:55]

.Lm_flush:
	s_nop 15
	v_div_scale_f32 v132, s[30:31], v42, v42, 1.0
	v_rcp_f32_e32 v133, v132
	v_div_scale_f32 v134, vcc, 1.0, v42, 1.0
	v_fma_f32 v135, -v132, v133, 1.0
	v_fmac_f32_e32 v133, v135, v133
	v_mul_f32_e32 v135, v134, v133
	v_fma_f32 v136, -v132, v135, v134
	v_fmac_f32_e32 v135, v136, v133
	v_fma_f32 v132, -v132, v135, v134
	s_mul_i32 s40, s29, 0x180
	s_lshl_b32 s41, s18, 5
	v_div_fmas_f32 v132, v132, v133, v135
	v_div_fixup_f32 v132, v132, v42, 1.0
	v_cmp_lt_f32_e32 vcc, 0, v42
	s_add_u32 s40, s40, s41
	s_lshl_b32 s44, s40, 2
	s_mul_i32 s45, s40, 0x68
	s_add_u32 s42, s16, s44
	s_addc_u32 s43, s17, 0
	v_cndmask_b32_e32 v130, 0, v132, vcc
	s_add_u32 s40, s14, s45
	s_addc_u32 s41, s15, 0
	v_mul_f32_e32 v132, v16, v130
	v_mul_f32_e32 v133, v17, v130
	v_mul_f32_e32 v134, v18, v130
	v_mul_f32_e32 v135, v19, v130
	v_cvt_pk_f16_f32 v136, v132, v133
	v_cvt_pk_f16_f32 v137, v134, v135
	ds_write_b64 v6, v[136:137] offset:0
	v_mul_f32_e32 v132, v20, v130
	v_mul_f32_e32 v133, v21, v130
	v_mul_f32_e32 v134, v22, v130
	v_mul_f32_e32 v135, v23, v130
	v_cvt_pk_f16_f32 v136, v132, v133
	v_cvt_pk_f16_f32 v137, v134, v135
	ds_write_b64 v6, v[136:137] offset:16
	v_mul_f32_e32 v132, v24, v130
	v_mul_f32_e32 v133, v25, v130
	v_mul_f32_e32 v134, v26, v130
	v_mul_f32_e32 v135, v27, v130
	v_cvt_pk_f16_f32 v136, v132, v133
	v_cvt_pk_f16_f32 v137, v134, v135
	ds_write_b64 v6, v[136:137] offset:32
	v_mul_f32_e32 v132, v28, v130
	v_mul_f32_e32 v133, v29, v130
	v_mul_f32_e32 v134, v30, v130
	v_mul_f32_e32 v135, v31, v130
	v_cvt_pk_f16_f32 v136, v132, v133
	v_cvt_pk_f16_f32 v137, v134, v135
	ds_write_b64 v6, v[136:137] offset:48
	v_mul_f32_e32 v132, v32, v130
	v_mul_f32_e32 v133, v33, v130
	v_mul_f32_e32 v134, v34, v130
	v_mul_f32_e32 v135, v35, v130
	v_cvt_pk_f16_f32 v136, v132, v133
	v_cvt_pk_f16_f32 v137, v134, v135
	ds_write_b64 v6, v[136:137] offset:64
	v_mul_f32_e32 v132, v36, v130
	v_mul_f32_e32 v133, v37, v130
	v_mul_f32_e32 v134, v38, v130
	v_mul_f32_e32 v135, v39, v130
	v_cvt_pk_f16_f32 v136, v132, v133
	v_cvt_pk_f16_f32 v137, v134, v135
	ds_write_b64 v6, v[136:137] offset:80
	s_mov_b32 exec_hi, 0
	v_mul_f32_e32 v132, v40, v130
	v_mul_f32_e32 v133, v41, v130
	v_mul_f32_e32 v134, v42, v130
	v_mul_f32_e32 v135, v43, v130
	v_cvt_pk_f16_f32 v136, v132, v133
	v_cvt_pk_f16_f32 v137, v134, v135
	ds_write_b64 v6, v[136:137] offset:96
	s_mov_b64 exec, -1
	s_waitcnt lgkmcnt(0)
	ds_read_b128 v[132:135], v7 offset:0
	ds_read_b128 v[136:139], v7 offset:1024
	ds_read_b128 v[140:143], v7 offset:2048
	ds_read_b128 v[144:147], v7 offset:3072
	v_log_f32_e32 v131, v42
	s_waitcnt lgkmcnt(0)
	v_sub_f32_e32 v131, v131, v148
	global_store_dwordx4 v2, v[132:135], s[40:41] offset:0 nt
	global_store_dwordx4 v2, v[136:139], s[40:41] offset:1024 nt
	global_store_dwordx4 v2, v[140:143], s[40:41] offset:2048 nt
	v_cndmask_b32_e32 v131, v150, v131, vcc
	s_mov_b32 exec_lo, 0xffff
	s_mov_b32 exec_hi, 0
	global_store_dwordx4 v2, v[144:147], s[40:41] offset:3072 nt
	s_mov_b32 exec_lo, -1
	global_store_dword v5, v131, s[42:43]
	s_mov_b64 exec, -1
	s_cmp_lt_u32 s27, 9
	s_cbranch_scc1 .Lm_switch
	s_endpgm

_Z11pam_combinePKDF16_PKfS2_S2_Pf:
	v_lshl_or_b32 v0, s2, 8, v0
	s_mov_b32 s2, 0x1f800
	v_cmp_gt_i32_e32 vcc, s2, v0
	s_and_saveexec_b64 s[2:3], vcc
	s_cbranch_execz .LBB2_3
	s_mov_b32 s2, 0x92492493
	v_mul_hi_i32 v1, v0, s2
	v_add_u32_e32 v1, v1, v0
	v_lshrrev_b32_e32 v2, 31, v1
	v_ashrrev_i32_e32 v1, 2, v1
	s_mov_b32 s2, 0x30c30c31
	v_add_u32_e32 v35, v1, v2
	v_mul_hi_i32 v1, v0, s2
	v_lshrrev_b32_e32 v2, 31, v1
	v_ashrrev_i32_e32 v1, 9, v1
	v_add_u32_e32 v1, v1, v2
	v_mul_i32_i24_e32 v2, 0x120, v1
	s_mov_b32 s3, 0x4bda12f7
	v_mul_hi_i32 v2, v2, s3
	s_movk_i32 s2, 0xfe80
	v_lshrrev_b32_e32 v3, 31, v2
	v_ashrrev_i32_e32 v2, 4, v2
	v_mad_i32_i24 v20, v1, s2, v35
	s_movk_i32 s2, 0x120
	v_add_u32_e32 v14, v2, v3
	v_mov_b32_e32 v2, 0x11f
	v_mad_i32_i24 v2, v1, s2, v2
	v_mul_hi_i32 v2, v2, s3
	v_lshrrev_b32_e32 v3, 31, v2
	v_ashrrev_i32_e32 v2, 4, v2
	v_add_u32_e32 v2, v2, v3
	v_sub_u32_e32 v34, v2, v14
	v_min_i32_e32 v2, 0, v34
	v_add_u32_e32 v2, v2, v14
	v_mul_lo_u32 v3, v2, 54
	s_mov_b32 s4, 0x38e38e39
	v_mul_hi_i32 v3, v3, s4
	v_lshrrev_b32_e32 v4, 31, v3
	v_ashrrev_i32_e32 v3, 6, v3
	v_add_u32_e32 v3, v3, v4
	v_min_i32_e32 v4, 1, v34
	v_add_u32_e32 v4, v4, v14
	v_mul_lo_u32 v5, v4, 54
	v_mul_hi_i32 v5, v5, s4
	v_lshrrev_b32_e32 v6, 31, v5
	v_ashrrev_i32_e32 v5, 6, v5
	v_add_u32_e32 v5, v5, v6
	v_min_i32_e32 v6, 2, v34
	v_add_u32_e32 v6, v6, v14
	v_mul_lo_u32 v7, v6, 54
	v_mul_hi_i32 v7, v7, s4
	v_lshrrev_b32_e32 v8, 31, v7
	v_ashrrev_i32_e32 v7, 6, v7
	v_add_u32_e32 v7, v7, v8
	v_min_i32_e32 v8, 3, v34
	v_add_u32_e32 v8, v8, v14
	v_mul_lo_u32 v9, v8, 54
	v_mul_hi_i32 v9, v9, s4
	v_lshrrev_b32_e32 v10, 31, v9
	v_ashrrev_i32_e32 v9, 6, v9
	v_add_u32_e32 v9, v9, v10
	v_min_i32_e32 v10, 4, v34
	v_add_u32_e32 v10, v10, v14
	v_mul_lo_u32 v11, v10, 54
	v_mul_hi_i32 v11, v11, s4
	v_lshrrev_b32_e32 v12, 31, v11
	v_ashrrev_i32_e32 v11, 6, v11
	v_add_u32_e32 v11, v11, v12
	v_min_i32_e32 v12, 5, v34
	v_add_u32_e32 v15, 0x100, v1
	v_cmp_eq_u32_e32 vcc, v3, v1
	v_add_u32_e32 v12, v12, v14
	v_mul_lo_u32 v13, v12, 54
	v_cndmask_b32_e32 v16, v15, v2, vcc
	v_cmp_eq_u32_e32 vcc, v5, v1
	v_mul_hi_i32 v13, v13, s4
	s_load_dwordx8 s[8:15], s[0:1], 0x0
	v_cndmask_b32_e32 v17, v15, v4, vcc
	v_cmp_eq_u32_e32 vcc, v7, v1
	v_lshrrev_b32_e32 v22, 31, v13
	v_ashrrev_i32_e32 v13, 6, v13
	v_cndmask_b32_e32 v18, v15, v6, vcc
	v_cmp_eq_u32_e32 vcc, v9, v1
	v_add_u32_e32 v13, v13, v22
	v_ashrrev_i32_e32 v21, 31, v20
	v_cndmask_b32_e32 v19, v15, v8, vcc
	v_cmp_eq_u32_e32 vcc, v11, v1
	s_movk_i32 s5, 0x180
	v_mad_u64_u32 v[4:5], s[2:3], v17, s5, v[20:21]
	v_cndmask_b32_e32 v26, v15, v10, vcc
	v_cmp_eq_u32_e32 vcc, v13, v1
	v_ashrrev_i32_e32 v5, 31, v4
	v_mad_u64_u32 v[6:7], s[2:3], v18, s5, v[20:21]
	v_cndmask_b32_e32 v30, v15, v12, vcc
	v_mad_u64_u32 v[8:9], s[2:3], v19, s5, v[20:21]
	v_mad_u64_u32 v[10:11], s[2:3], v26, s5, v[20:21]
	v_mad_u64_u32 v[12:13], s[2:3], v30, s5, v[20:21]
	s_waitcnt lgkmcnt(0)
	v_mad_i32_i24 v68, v35, -7, v0
	v_mul_u32_u24_e32 v69, 0xc8, v35
	v_cmp_gt_i32_e32 vcc, 6, v68
	v_lshl_add_u32 v69, v68, 5, v69
	v_cndmask_b32_e64 v76, 0, 8, vcc
	global_load_dwordx2 v[70:71], v69, s[12:13]
	v_add_u32_e32 v77, v69, v76
	v_lshl_add_u32 v78, v76, 1, v69
	v_mad_u32_u24 v79, v76, 3, v69
	global_load_dwordx2 v[72:73], v77, s[12:13]
	global_load_dwordx2 v[74:75], v78, s[12:13]
	global_load_dwordx2 v[80:81], v79, s[12:13]
	v_lshl_add_u64 v[4:5], v[4:5], 2, s[10:11]
	v_ashrrev_i32_e32 v7, 31, v6
	v_ashrrev_i32_e32 v9, 31, v8
	v_ashrrev_i32_e32 v11, 31, v10
	v_ashrrev_i32_e32 v13, 31, v12
	v_lshl_add_u64 v[6:7], v[6:7], 2, s[10:11]
	v_lshl_add_u64 v[8:9], v[8:9], 2, s[10:11]
	v_lshl_add_u64 v[10:11], v[10:11], 2, s[10:11]
	v_lshl_add_u64 v[12:13], v[12:13], 2, s[10:11]
	global_load_dword v36, v[4:5], off
	global_load_dword v37, v[6:7], off
	global_load_dword v38, v[8:9], off
	global_load_dword v39, v[10:11], off
	global_load_dword v41, v[12:13], off
	v_min_i32_e32 v4, 6, v34
	v_add_u32_e32 v4, v4, v14
	v_mul_lo_u32 v5, v4, 54
	v_mul_hi_i32 v5, v5, s4
	v_lshrrev_b32_e32 v6, 31, v5
	v_ashrrev_i32_e32 v5, 6, v5
	v_add_u32_e32 v5, v5, v6
	v_cmp_eq_u32_e32 vcc, v5, v1
	v_mad_u64_u32 v[2:3], s[2:3], v16, s5, v[20:21]
	s_nop 0
	v_cndmask_b32_e32 v32, v15, v4, vcc
	v_mad_u64_u32 v[4:5], s[2:3], v32, s5, v[20:21]
	v_ashrrev_i32_e32 v5, 31, v4
	v_ashrrev_i32_e32 v3, 31, v2
	v_lshl_add_u64 v[4:5], v[4:5], 2, s[10:11]
	v_lshl_add_u64 v[2:3], v[2:3], 2, s[10:11]
	global_load_dword v43, v[4:5], off
	global_load_dword v40, v[2:3], off
	v_mad_u64_u32 v[44:45], s[2:3], v35, -7, v[0:1]
	v_lshlrev_b32_e32 v28, 3, v44
	v_ashrrev_i32_e32 v29, 31, v28
	v_lshl_add_u64 v[22:23], v[28:29], 1, s[8:9]
	v_mad_i64_i32 v[0:1], s[2:3], v16, s5, v[20:21]
	s_movk_i32 s4, 0x68
	v_mad_u64_u32 v[2:3], s[2:3], v0, s4, v[22:23]
	v_mad_i64_i32 v[4:5], s[2:3], v17, s5, v[20:21]
	v_mad_i32_i24 v3, v1, s4, v3
	v_mad_u64_u32 v[12:13], s[2:3], v4, s4, v[22:23]
	global_load_dwordx4 v[0:3], v[2:3], off nt
	v_mad_i32_i24 v13, v5, s4, v13
	v_mad_i64_i32 v[4:5], s[2:3], v18, s5, v[20:21]
	v_mad_u64_u32 v[14:15], s[2:3], v4, s4, v[22:23]
	v_mad_i32_i24 v15, v5, s4, v15
	global_load_dwordx4 v[4:7], v[12:13], off nt
	global_load_dwordx4 v[8:11], v[14:15], off nt
	v_mad_i64_i32 v[12:13], s[2:3], v19, s5, v[20:21]
	v_mad_u64_u32 v[24:25], s[2:3], v12, s4, v[22:23]
	v_mad_i32_i24 v25, v13, s4, v25
	v_mad_i64_i32 v[12:13], s[2:3], v26, s5, v[20:21]
	v_mad_u64_u32 v[26:27], s[2:3], v12, s4, v[22:23]
	v_mad_i32_i24 v27, v13, s4, v27
	global_load_dwordx4 v[12:15], v[24:25], off nt
	global_load_dwordx4 v[16:19], v[26:27], off nt
	v_mad_i64_i32 v[24:25], s[2:3], v30, s5, v[20:21]
	v_mad_u64_u32 v[30:31], s[2:3], v24, s4, v[22:23]
	v_mad_i64_i32 v[20:21], s[2:3], v32, s5, v[20:21]
	v_mad_i32_i24 v31, v25, s4, v31
	v_mad_u64_u32 v[32:33], s[2:3], v20, s4, v[22:23]
	v_mad_i32_i24 v33, v21, s4, v33
	global_load_dwordx4 v[20:23], v[30:31], off nt
	global_load_dwordx4 v[24:27], v[32:33], off nt
	s_movk_i32 s16, 0xc8
	v_mov_b64_e32 v[30:31], s[12:13]
	v_mad_i64_i32 v[30:31], s[2:3], v35, s16, v[30:31]
	v_lshlrev_b64 v[46:47], 2, v[28:29]
	v_lshl_add_u64 v[28:29], v[30:31], 0, v[46:47]
	v_mov_b32_e32 v30, 0xff61b1e6
	v_cmp_gt_i32_e32 vcc, 1, v34
	v_cmp_gt_i32_e64 s[2:3], 2, v34
	v_cmp_gt_i32_e64 s[4:5], 3, v34
	v_cmp_gt_i32_e64 s[6:7], 4, v34
	v_cmp_gt_i32_e64 s[8:9], 5, v34
	v_cmp_gt_i32_e64 s[10:11], 6, v34
	v_cmp_gt_i32_e64 s[12:13], 0, v34
	s_waitcnt vmcnt(13)
	v_cndmask_b32_e32 v31, v36, v30, vcc
	s_waitcnt vmcnt(12)
	v_cndmask_b32_e64 v32, v37, v30, s[2:3]
	s_waitcnt vmcnt(11)
	v_cndmask_b32_e64 v33, v38, v30, s[4:5]
	s_waitcnt vmcnt(10)
	v_cndmask_b32_e64 v42, v39, v30, s[6:7]
	s_waitcnt vmcnt(9)
	v_cndmask_b32_e64 v45, v41, v30, s[8:9]
	s_waitcnt vmcnt(8)
	v_cndmask_b32_e64 v50, v43, v30, s[10:11]
	s_waitcnt vmcnt(7)
	v_max_f32_e32 v48, v40, v40
	v_max_f32_e32 v51, 0xff61b1e6, v48
	v_cndmask_b32_e64 v30, v51, v30, s[12:13]
	v_max3_f32 v30, v30, v31, v32
	v_max3_f32 v30, v30, v33, v42
	v_max3_f32 v30, v30, v45, v50
	v_sub_f32_e32 v31, v40, v30
	v_exp_f32_e32 v31, v31
	v_sub_f32_e32 v32, v37, v30
	v_exp_f32_e32 v32, v32
	v_cndmask_b32_e64 v42, v31, 0, s[12:13]
	v_sub_f32_e32 v31, v36, v30
	v_exp_f32_e32 v31, v31
	v_cndmask_b32_e64 v34, v32, 0, s[2:3]
	v_sub_f32_e32 v32, v38, v30
	v_add_f32_e32 v33, 0, v42
	v_cndmask_b32_e64 v36, v31, 0, vcc
	v_exp_f32_e32 v32, v32
	v_add_f32_e32 v31, v33, v36
	v_sub_f32_e32 v33, v39, v30
	v_exp_f32_e32 v33, v33
	v_cndmask_b32_e64 v40, v32, 0, s[4:5]
	v_sub_f32_e32 v32, v41, v30
	v_exp_f32_e32 v32, v32
	v_sub_f32_e32 v30, v43, v30
	v_cndmask_b32_e64 v38, v33, 0, s[6:7]
	v_exp_f32_e32 v33, v30
	v_add_f32_e32 v31, v31, v34
	v_add_f32_e32 v31, v31, v40
	v_add_f32_e32 v31, v31, v38
	v_cndmask_b32_e64 v30, v32, 0, s[8:9]
	v_add_f32_e32 v31, v31, v30
	v_cndmask_b32_e64 v32, v33, 0, s[10:11]
	v_add_f32_e32 v31, v31, v32
	v_div_scale_f32 v33, s[2:3], v31, v31, 1.0
	v_rcp_f32_e32 v37, v33
	s_waitcnt vmcnt(6)
	v_cvt_f32_f16_e32 v56, v0
	v_cvt_f32_f16_sdwa v57, v0 dst_sel:DWORD dst_unused:UNUSED_PAD src0_sel:WORD_1
	s_waitcnt vmcnt(5)
	v_cvt_f32_f16_e32 v54, v4
	v_fma_f32 v39, -v33, v37, 1.0
	v_fmac_f32_e32 v37, v39, v37
	v_div_scale_f32 v39, vcc, 1.0, v31, 1.0
	v_cvt_f32_f16_sdwa v55, v4 dst_sel:DWORD dst_unused:UNUSED_PAD src0_sel:WORD_1
	s_load_dwordx2 s[4:5], s[0:1], 0x20
	v_mul_f32_e32 v41, v39, v37
	s_waitcnt vmcnt(4)
	v_cvt_f32_f16_e32 v58, v8
	v_cvt_f32_f16_sdwa v59, v8 dst_sel:DWORD dst_unused:UNUSED_PAD src0_sel:WORD_1
	v_fma_f32 v43, -v33, v41, v39
	v_pk_fma_f32 v[56:57], v[42:43], v[56:57], 0 op_sel_hi:[0,1,0]
	v_pk_fma_f32 v[54:55], v[36:37], v[54:55], v[56:57] op_sel_hi:[0,1,1]
	v_pk_fma_f32 v[54:55], v[34:35], v[58:59], v[54:55] op_sel_hi:[0,1,1]
	s_waitcnt vmcnt(3)
	v_cvt_f32_f16_e32 v58, v12
	v_cvt_f32_f16_sdwa v59, v12 dst_sel:DWORD dst_unused:UNUSED_PAD src0_sel:WORD_1
	s_waitcnt lgkmcnt(0)
	v_mov_b64_e32 v[50:51], s[4:5]
	s_waitcnt vmcnt(2)
	v_cvt_f32_f16_e32 v56, v16
	v_cvt_f32_f16_sdwa v57, v16 dst_sel:DWORD dst_unused:UNUSED_PAD src0_sel:WORD_1
	v_mad_i64_i32 v[50:51], s[4:5], v35, s16, v[50:51]
	s_waitcnt vmcnt(1)
	v_cvt_f32_f16_e32 v52, v20
	v_cvt_f32_f16_sdwa v53, v20 dst_sel:DWORD dst_unused:UNUSED_PAD src0_sel:WORD_1
	v_fmac_f32_e32 v41, v43, v37
	v_lshl_add_u64 v[46:47], v[50:51], 0, v[46:47]
	s_waitcnt vmcnt(0)
	v_cvt_f32_f16_e32 v50, v24
	v_cvt_f32_f16_sdwa v51, v24 dst_sel:DWORD dst_unused:UNUSED_PAD src0_sel:WORD_1
	s_load_dword s2, s[14:15], 0x0
	v_pk_fma_f32 v[54:55], v[40:41], v[58:59], v[54:55] op_sel_hi:[0,1,1]
	v_fma_f32 v33, -v33, v41, v39
	v_pk_fma_f32 v[54:55], v[38:39], v[56:57], v[54:55] op_sel_hi:[0,1,1]
	v_div_fmas_f32 v33, v33, v37, v41
	v_pk_fma_f32 v[52:53], v[30:31], v[52:53], v[54:55] op_sel_hi:[0,1,1]
	v_cmp_gt_i32_e64 s[0:1], 6, v44
	v_div_fixup_f32 v44, v33, v31, 1.0
	v_pk_fma_f32 v[50:51], v[32:33], v[50:51], v[52:53] op_sel_hi:[0,1,1]
	v_pk_mul_f32 v[50:51], v[44:45], v[50:51] op_sel_hi:[0,1]
	s_waitcnt vmcnt(0) lgkmcnt(0)
	v_pk_fma_f32 v[48:49], s[2:3], v[50:51], v[70:71] op_sel_hi:[0,1,1]
	global_store_dwordx2 v[46:47], v[48:49], off
	s_and_b64 exec, exec, s[0:1]
	s_cbranch_execz .LBB2_3
	v_cvt_f32_f16_sdwa v49, v25 dst_sel:DWORD dst_unused:UNUSED_PAD src0_sel:WORD_1
	v_cvt_f32_f16_e32 v48, v25
	v_cvt_f32_f16_sdwa v25, v21 dst_sel:DWORD dst_unused:UNUSED_PAD src0_sel:WORD_1
	v_cvt_f32_f16_e32 v24, v21
	v_cvt_f32_f16_sdwa v21, v17 dst_sel:DWORD dst_unused:UNUSED_PAD src0_sel:WORD_1
	v_cvt_f32_f16_e32 v20, v17
	v_cvt_f32_f16_sdwa v17, v13 dst_sel:DWORD dst_unused:UNUSED_PAD src0_sel:WORD_1
	v_cvt_f32_f16_e32 v16, v13
	v_cvt_f32_f16_sdwa v13, v26 dst_sel:DWORD dst_unused:UNUSED_PAD src0_sel:WORD_1
	v_cvt_f32_f16_e32 v12, v26
	v_cvt_f32_f16_sdwa v51, v27 dst_sel:DWORD dst_unused:UNUSED_PAD src0_sel:WORD_1
	v_cvt_f32_f16_e32 v50, v27
	v_cvt_f32_f16_sdwa v27, v22 dst_sel:DWORD dst_unused:UNUSED_PAD src0_sel:WORD_1
	v_cvt_f32_f16_e32 v26, v22
	v_cvt_f32_f16_sdwa v53, v23 dst_sel:DWORD dst_unused:UNUSED_PAD src0_sel:WORD_1
	v_cvt_f32_f16_e32 v52, v23
	v_cvt_f32_f16_sdwa v23, v18 dst_sel:DWORD dst_unused:UNUSED_PAD src0_sel:WORD_1
	v_cvt_f32_f16_e32 v22, v18
	v_cvt_f32_f16_sdwa v55, v19 dst_sel:DWORD dst_unused:UNUSED_PAD src0_sel:WORD_1
	v_cvt_f32_f16_e32 v54, v19
	v_cvt_f32_f16_sdwa v19, v14 dst_sel:DWORD dst_unused:UNUSED_PAD src0_sel:WORD_1
	v_cvt_f32_f16_e32 v18, v14
	v_cvt_f32_f16_sdwa v57, v15 dst_sel:DWORD dst_unused:UNUSED_PAD src0_sel:WORD_1
	v_cvt_f32_f16_e32 v56, v15
	v_cvt_f32_f16_sdwa v15, v9 dst_sel:DWORD dst_unused:UNUSED_PAD src0_sel:WORD_1
	v_cvt_f32_f16_e32 v14, v9
	v_cvt_f32_f16_sdwa v9, v10 dst_sel:DWORD dst_unused:UNUSED_PAD src0_sel:WORD_1
	v_cvt_f32_f16_e32 v8, v10
	v_cvt_f32_f16_sdwa v59, v11 dst_sel:DWORD dst_unused:UNUSED_PAD src0_sel:WORD_1
	v_cvt_f32_f16_e32 v58, v11
	v_cvt_f32_f16_sdwa v11, v5 dst_sel:DWORD dst_unused:UNUSED_PAD src0_sel:WORD_1
	v_cvt_f32_f16_e32 v10, v5
	v_cvt_f32_f16_sdwa v5, v6 dst_sel:DWORD dst_unused:UNUSED_PAD src0_sel:WORD_1
	v_cvt_f32_f16_e32 v4, v6
	v_cvt_f32_f16_sdwa v61, v7 dst_sel:DWORD dst_unused:UNUSED_PAD src0_sel:WORD_1
	v_cvt_f32_f16_e32 v60, v7
	v_cvt_f32_f16_sdwa v7, v1 dst_sel:DWORD dst_unused:UNUSED_PAD src0_sel:WORD_1
	v_cvt_f32_f16_e32 v6, v1
	v_cvt_f32_f16_sdwa v1, v2 dst_sel:DWORD dst_unused:UNUSED_PAD src0_sel:WORD_1
	v_cvt_f32_f16_e32 v0, v2
	v_cvt_f32_f16_sdwa v63, v3 dst_sel:DWORD dst_unused:UNUSED_PAD src0_sel:WORD_1
	v_cvt_f32_f16_e32 v62, v3
	v_cndmask_b32_e64 v2, 0, 8, s[0:1]
	v_mov_b32_e32 v3, 0
	v_lshl_add_u64 v[64:65], v[28:29], 0, v[2:3]
	v_cndmask_b32_e64 v2, 0, 16, s[0:1]
	v_mov_b32_e32 v43, v42
	v_lshl_add_u64 v[66:67], v[28:29], 0, v[2:3]
	v_cndmask_b32_e64 v2, 0, 24, s[0:1]
	v_mov_b32_e32 v37, v36
	v_pk_fma_f32 v[6:7], v[42:43], v[6:7], 0 op_sel_hi:[1,1,0]
	v_pk_fma_f32 v[0:1], v[42:43], v[0:1], 0 op_sel_hi:[1,1,0]
	v_lshl_add_u64 v[2:3], v[28:29], 0, v[2:3]
	v_pk_fma_f32 v[6:7], v[36:37], v[10:11], v[6:7]
	v_pk_fma_f32 v[0:1], v[36:37], v[4:5], v[0:1]
	v_pk_fma_f32 v[4:5], v[42:43], v[62:63], 0 op_sel_hi:[1,1,0]
	v_mov_b32_e32 v35, v34
	v_mov_b32_e32 v41, v40
	v_pk_fma_f32 v[2:3], v[36:37], v[60:61], v[4:5]
	v_pk_fma_f32 v[4:5], v[34:35], v[14:15], v[6:7]
	v_pk_fma_f32 v[0:1], v[34:35], v[8:9], v[0:1]
	v_mov_b32_e32 v39, v38
	v_pk_fma_f32 v[2:3], v[34:35], v[58:59], v[2:3]
	v_pk_fma_f32 v[4:5], v[40:41], v[16:17], v[4:5]
	v_pk_fma_f32 v[0:1], v[40:41], v[18:19], v[0:1]
	v_mov_b32_e32 v31, v30
	v_pk_fma_f32 v[2:3], v[40:41], v[56:57], v[2:3]
	v_pk_fma_f32 v[4:5], v[38:39], v[20:21], v[4:5]
	v_pk_fma_f32 v[0:1], v[38:39], v[22:23], v[0:1]
	v_mov_b32_e32 v33, v32
	v_pk_fma_f32 v[6:7], v[38:39], v[54:55], v[2:3]
	v_pk_fma_f32 v[2:3], v[30:31], v[24:25], v[4:5]
	v_pk_fma_f32 v[0:1], v[30:31], v[26:27], v[0:1]
	v_mov_b32_e32 v45, v44
	v_pk_fma_f32 v[2:3], v[32:33], v[48:49], v[2:3]
	v_pk_fma_f32 v[0:1], v[32:33], v[12:13], v[0:1]
	s_mov_b32 s3, s2
	v_pk_mul_f32 v[2:3], v[44:45], v[2:3]
	v_pk_mul_f32 v[4:5], v[44:45], v[0:1]
	v_pk_fma_f32 v[0:1], s[2:3], v[2:3], v[72:73]
	v_pk_fma_f32 v[2:3], s[2:3], v[4:5], v[74:75]
	global_store_dwordx4 v[46:47], v[0:3], off offset:8
	s_nop 1
	v_pk_fma_f32 v[0:1], v[30:31], v[52:53], v[6:7]
	s_nop 0
	v_pk_fma_f32 v[0:1], v[32:33], v[50:51], v[0:1]
	s_nop 0
	v_pk_mul_f32 v[0:1], v[44:45], v[0:1]
	v_pk_fma_f32 v[0:1], s[2:3], v[0:1], v[80:81]
	global_store_dwordx2 v[46:47], v[0:1], off offset:24

	.amdhsa_kernel _Z11pam_combinePKDF16_PKfS2_S2_Pf
		.amdhsa_group_segment_fixed_size 0
		.amdhsa_private_segment_fixed_size 0
		.amdhsa_kernarg_size 40
		.amdhsa_user_sgpr_count 2
		.amdhsa_user_sgpr_dispatch_ptr 0
		.amdhsa_user_sgpr_queue_ptr 0
		.amdhsa_user_sgpr_kernarg_segment_ptr 1
		.amdhsa_user_sgpr_dispatch_id 0
		.amdhsa_user_sgpr_kernarg_preload_length 0
		.amdhsa_user_sgpr_kernarg_preload_offset 0
		.amdhsa_user_sgpr_private_segment_size 0
		.amdhsa_uses_dynamic_stack 0
		.amdhsa_enable_private_segment 0
		.amdhsa_system_sgpr_workgroup_id_x 1
		.amdhsa_system_sgpr_workgroup_id_y 0
		.amdhsa_system_sgpr_workgroup_id_z 0
		.amdhsa_system_sgpr_workgroup_info 0
		.amdhsa_system_vgpr_workitem_id 0
		.amdhsa_next_free_vgpr 84
		.amdhsa_next_free_sgpr 17
		.amdhsa_accum_offset 84
		.amdhsa_reserve_vcc 1
		.amdhsa_float_round_mode_32 0
		.amdhsa_float_round_mode_16_64 0
		.amdhsa_float_denorm_mode_32 3
		.amdhsa_float_denorm_mode_16_64 3
		.amdhsa_dx10_clamp 1
		.amdhsa_ieee_mode 1
		.amdhsa_fp16_overflow 0
		.amdhsa_tg_split 0
		.amdhsa_exception_fp_ieee_invalid_op 0
		.amdhsa_exception_fp_denorm_src 0
		.amdhsa_exception_fp_ieee_div_zero 0
		.amdhsa_exception_fp_ieee_overflow 0
		.amdhsa_exception_fp_ieee_underflow 0
		.amdhsa_exception_fp_ieee_inexact 0
		.amdhsa_exception_int_div_zero 0
	.end_amdhsa_kernel

amdhsa.kernels:
  - .agpr_count:     16
    .args:
      - .actual_access:  read_only
        .address_space:  global
        .offset:         0
        .size:           8
        .value_kind:     global_buffer
      - .actual_access:  read_only
        .address_space:  global
        .offset:         8
        .size:           8
        .value_kind:     global_buffer
      - .actual_access:  read_only
        .address_space:  global
        .offset:         16
        .size:           8
        .value_kind:     global_buffer
      - .actual_access:  read_only
        .address_space:  global
        .offset:         24
        .size:           8
        .value_kind:     global_buffer
      - .actual_access:  write_only
        .address_space:  global
        .offset:         32
        .size:           8
        .value_kind:     global_buffer
      - .actual_access:  write_only
        .address_space:  global
        .offset:         40
        .size:           8
        .value_kind:     global_buffer
      - .actual_access:  write_only
        .address_space:  global
        .offset:         48
        .size:           8
        .value_kind:     global_buffer
      - .actual_access:  write_only
        .address_space:  global
        .offset:         56
        .size:           8
        .value_kind:     global_buffer
      - .actual_access:  write_only
        .address_space:  global
        .offset:         64
        .size:           8
        .value_kind:     global_buffer
    .group_segment_fixed_size: 29184
    .kernarg_segment_align: 8
    .kernarg_segment_size: 72
    .language:       OpenCL C
    .language_version:
      - 2
      - 0
    .max_flat_workgroup_size: 256
    .name:           _Z8pam_prepPKfS0_S0_S0_PDv4_jS2_S2_PfS3_
    .private_segment_fixed_size: 0
    .sgpr_count:     28
    .sgpr_spill_count: 0
    .symbol:         _Z8pam_prepPKfS0_S0_S0_PDv4_jS2_S2_PfS3_.kd
    .uniform_work_group_size: 1
    .uses_dynamic_stack: false
    .vgpr_count:     52
    .vgpr_spill_count: 0
    .wavefront_size: 64
  - .agpr_count:     0
    .args:
      - .address_space:  global
        .offset:         0
        .size:           8
        .value_kind:     global_buffer
      - .actual_access:  read_only
        .address_space:  global
        .offset:         8
        .size:           8
        .value_kind:     global_buffer
      - .address_space:  global
        .offset:         16
        .size:           8
        .value_kind:     global_buffer
      - .actual_access:  read_only
        .address_space:  global
        .offset:         24
        .size:           8
        .value_kind:     global_buffer
      - .actual_access:  read_only
        .address_space:  global
        .offset:         32
        .size:           8
        .value_kind:     global_buffer
      - .actual_access:  write_only
        .address_space:  global
        .offset:         40
        .size:           8
        .value_kind:     global_buffer
      - .actual_access:  write_only
        .address_space:  global
        .offset:         48
        .size:           8
        .value_kind:     global_buffer
    .group_segment_fixed_size: 133120
    .kernarg_segment_align: 8
    .kernarg_segment_size: 56
    .language:       OpenCL C
    .language_version:
      - 2
      - 0
    .max_flat_workgroup_size: 768
    .name:           _Z8pam_mainPKDv4_jS1_S1_PKfS3_PDF16_Pf
    .private_segment_fixed_size: 0
    .sgpr_count:     52
    .sgpr_spill_count: 0
    .symbol:         _Z8pam_mainPKDv4_jS1_S1_PKfS3_PDF16_Pf.kd
    .uniform_work_group_size: 1
    .uses_dynamic_stack: false
    .vgpr_count:     152
    .vgpr_spill_count: 0
    .wavefront_size: 64
  - .agpr_count:     0
    .args:
      - .actual_access:  read_only
        .address_space:  global
        .offset:         0
        .size:           8
        .value_kind:     global_buffer
      - .actual_access:  read_only
        .address_space:  global
        .offset:         8
        .size:           8
        .value_kind:     global_buffer
      - .actual_access:  read_only
        .address_space:  global
        .offset:         16
        .size:           8
        .value_kind:     global_buffer
      - .actual_access:  read_only
        .address_space:  global
        .offset:         24
        .size:           8
        .value_kind:     global_buffer
      - .actual_access:  write_only
        .address_space:  global
        .offset:         32
        .size:           8
        .value_kind:     global_buffer
    .group_segment_fixed_size: 0
    .kernarg_segment_align: 8
    .kernarg_segment_size: 40
    .language:       OpenCL C
    .language_version:
      - 2
      - 0
    .max_flat_workgroup_size: 256
    .name:           _Z11pam_combinePKDF16_PKfS2_S2_Pf
    .private_segment_fixed_size: 0
    .sgpr_count:     23
    .sgpr_spill_count: 0
    .symbol:         _Z11pam_combinePKDF16_PKfS2_S2_Pf.kd
    .uniform_work_group_size: 1
    .uses_dynamic_stack: false
    .vgpr_count:     84
    .vgpr_spill_count: 0
    .wavefront_size: 64
